# speedup vs baseline: 1.0044x; 1.0044x over previous
.LBB1_26:
	s_and_b64 vcc, exec, s[68:69]
	s_cbranch_vccz .Lt_nw
	v_mov_b32_e32 v2, 0x24800
	v_lshl_add_u32 v2, v0, 2, v2
	ds_write_b32 v2, v137
.Lt_nw:
	s_waitcnt vmcnt(0) lgkmcnt(0)
	s_barrier
